# attention: hand-scheduled unmasked key-tile body with coarse LDS waits, V^T fragments as ds_read_b128 (144-byte rows), dead default copies removed; up GEMMs: one K trip for kv-up and lora units (skip
# speedup vs baseline: 1.0124x; 1.0124x over previous
.LBB0_658:
	s_lshl_b32 s10, s42, 17
	s_add_i32 s49, s12, s10
	s_cmp_eq_u32 s45, 2
	s_cselect_b32 s10, 0x100, 0
	s_cmp_eq_u32 s42, 2
	s_cselect_b32 s10, s10, 0
	s_add_i32 s49, s49, s10

.LBB0_695:
	s_lshl_b32 s10, s48, 13
	s_and_b32 s10, s10, 0x2000
	v_add_u32_e32 v144, s10, v140
	s_lshl_b32 s10, s39, 13
	s_and_b32 s10, s10, 0x2000
	v_add_u32_e32 v131, v131, v139
	s_cmp_eq_u32 s45, 2
	s_cselect_b32 s51, 0x100, 0
	s_cmp_eq_u32 s42, 2
	s_cselect_b32 s51, s51, 0
	v_add_u32_e32 v128, s51, v128
	v_add_u32_e32 v129, s51, v129
	v_add_u32_e32 v130, s51, v130
	v_add_u32_e32 v131, s51, v131
	s_bitcmp1_b32 s39, 0
	ds_write_b128 v144, v[128:131]
	v_add_u32_e32 v128, s10, v140
	s_mov_b32 s50, 0
	s_mov_b64 s[12:13], -1
	s_mov_b64 s[14:15], 0
	s_cselect_b64 s[10:11], -1, 0
	s_cmp_eq_u32 s44, 0
	s_cbranch_scc1 .Lup_long
	s_mov_b64 s[12:13], 0
	s_mov_b64 s[14:15], -1
.Lup_long:
.LBB0_696:
	ds_read_b128 v[144:147], v142
	ds_read_b128 v[148:151], v142 offset:1024
	ds_read_b128 v[152:155], v142 offset:2048
	ds_read_b128 v[156:159], v142 offset:3072
	ds_read_b128 v[160:163], v142 offset:16384
	ds_read_b128 v[164:167], v142 offset:17408
	ds_read_b128 v[168:171], v142 offset:18432
	ds_read_b128 v[172:175], v142 offset:19456
	s_add_i32 s51, s50, 0x100
	s_add_i32 s54, s51, s21
	s_and_b64 s[52:53], s[14:15], exec
	s_cselect_b32 s54, s49, s54
	s_cselect_b32 s53, 0, s51
	s_add_i32 s51, s54, 0x80
	s_or_b32 s59, s50, 0x80
	s_add_i32 s57, s54, 0x8000
	s_add_i32 s56, s54, 0x10000
	s_add_i32 s55, s54, 0x18000
	s_xor_b64 s[14:15], s[14:15], s[10:11]
	s_and_b64 s[14:15], s[14:15], exec
	s_cselect_b32 s58, 0x2000, 0
	s_or_b32 s14, s53, 0x80
	s_add_i32 s50, s54, 0x10080
	s_add_i32 s15, s54, 0x18080
	s_add_i32 s52, s54, 0x8080
	ds_read_b128 v[176:179], v143 offset:1024
	ds_read_b128 v[180:183], v143 offset:2048
	ds_read_b128 v[184:187], v143 offset:3072
	ds_read_b128 v[188:191], v143 offset:4096
	ds_read_b128 v[192:195], v143
	ds_read_b64 v[130:131], v128 offset:8
	ds_read_b128 v[196:199], v143 offset:5120
	ds_read_b128 v[200:203], v143 offset:6144
	ds_read_b128 v[204:207], v143 offset:7168
	s_mov_b32 s60, s2
	s_mov_b32 m0, s34
	s_waitcnt lgkmcnt(3)
	buffer_load_dwordx4 v130, s[60:63], s59 offen lds
	s_mov_b32 m0, s35
	s_nop 0
	buffer_load_dwordx4 v131, s[60:63], s59 offen lds
	s_waitcnt vmcnt(8)
	s_waitcnt lgkmcnt(0)
	s_barrier
	s_setprio 1
	v_mfma_f32_16x16x32_bf16 v[124:127], v[144:147], v[192:195], v[124:127]
	v_mfma_f32_16x16x32_bf16 v[120:123], v[152:155], v[192:195], v[120:123]
	v_mfma_f32_16x16x32_bf16 v[116:119], v[144:147], v[180:183], v[116:119]
	v_mfma_f32_16x16x32_bf16 v[112:115], v[152:155], v[180:183], v[112:115]
	v_mfma_f32_16x16x32_bf16 v[108:111], v[144:147], v[188:191], v[108:111]
	v_mfma_f32_16x16x32_bf16 v[104:107], v[152:155], v[188:191], v[104:107]
	s_waitcnt lgkmcnt(1)
	v_mfma_f32_16x16x32_bf16 v[100:103], v[144:147], v[200:203], v[100:103]
	v_mfma_f32_16x16x32_bf16 v[96:99], v[152:155], v[200:203], v[96:99]
	v_mfma_f32_16x16x32_bf16 v[124:127], v[148:151], v[176:179], v[124:127]
	v_mfma_f32_16x16x32_bf16 v[120:123], v[156:159], v[176:179], v[120:123]
	v_mfma_f32_16x16x32_bf16 v[116:119], v[148:151], v[184:187], v[116:119]
	v_mfma_f32_16x16x32_bf16 v[112:115], v[156:159], v[184:187], v[112:115]
	v_mfma_f32_16x16x32_bf16 v[108:111], v[148:151], v[196:199], v[108:111]
	v_mfma_f32_16x16x32_bf16 v[104:107], v[156:159], v[196:199], v[104:107]
	s_waitcnt lgkmcnt(0)
	v_mfma_f32_16x16x32_bf16 v[100:103], v[148:151], v[204:207], v[100:103]
	v_mfma_f32_16x16x32_bf16 v[96:99], v[156:159], v[204:207], v[96:99]
	s_setprio 0
	s_setprio 1
	v_mfma_f32_16x16x32_bf16 v[92:95], v[160:163], v[192:195], v[92:95]
	v_mfma_f32_16x16x32_bf16 v[88:91], v[168:171], v[192:195], v[88:91]
	v_mfma_f32_16x16x32_bf16 v[84:87], v[160:163], v[180:183], v[84:87]
	v_mfma_f32_16x16x32_bf16 v[80:83], v[168:171], v[180:183], v[80:83]
	v_mfma_f32_16x16x32_bf16 v[76:79], v[160:163], v[188:191], v[76:79]
	v_mfma_f32_16x16x32_bf16 v[72:75], v[168:171], v[188:191], v[72:75]
	v_mfma_f32_16x16x32_bf16 v[68:71], v[160:163], v[200:203], v[68:71]
	v_mfma_f32_16x16x32_bf16 v[64:67], v[168:171], v[200:203], v[64:67]
	v_mfma_f32_16x16x32_bf16 v[92:95], v[164:167], v[176:179], v[92:95]
	v_mfma_f32_16x16x32_bf16 v[88:91], v[172:175], v[176:179], v[88:91]
	v_mfma_f32_16x16x32_bf16 v[84:87], v[164:167], v[184:187], v[84:87]
	v_mfma_f32_16x16x32_bf16 v[80:83], v[172:175], v[184:187], v[80:83]
	v_mfma_f32_16x16x32_bf16 v[76:79], v[164:167], v[196:199], v[76:79]
	v_mfma_f32_16x16x32_bf16 v[72:75], v[172:175], v[196:199], v[72:75]
	v_mfma_f32_16x16x32_bf16 v[68:71], v[164:167], v[204:207], v[68:71]
	v_mfma_f32_16x16x32_bf16 v[64:67], v[172:175], v[204:207], v[64:67]
	s_setprio 0
	s_barrier
	s_mov_b32 m0, s17
	ds_read_b128 v[176:179], v143 offset:16384
	ds_read_b128 v[180:183], v143 offset:17408
	ds_read_b128 v[184:187], v143 offset:18432
	ds_read_b128 v[188:191], v143 offset:19456
	ds_read_b128 v[192:195], v143 offset:20480
	ds_read_b128 v[196:199], v143 offset:21504
	ds_read_b128 v[200:203], v143 offset:22528
	ds_read_b128 v[204:207], v143 offset:23552
	buffer_load_dwordx4 v141, s[60:63], s54 offen lds
	s_mov_b32 m0, s18
	v_add_u32_e32 v129, s58, v140
	buffer_load_dwordx4 v141, s[60:63], s57 offen lds
	s_mov_b32 m0, s19
	s_nop 0
	buffer_load_dwordx4 v141, s[60:63], s56 offen lds
	s_mov_b32 m0, s20
	s_nop 0
	buffer_load_dwordx4 v141, s[60:63], s55 offen lds
	ds_read_b64 v[130:131], v129
	s_mov_b32 m0, s16
	s_waitcnt lgkmcnt(0)
	buffer_load_dwordx4 v130, s[60:63], s53 offen lds
	s_mov_b32 m0, s22
	s_nop 0
	buffer_load_dwordx4 v131, s[60:63], s53 offen lds
	s_waitcnt vmcnt(8)
	s_waitcnt lgkmcnt(0)
	s_barrier
	s_setprio 1
	v_mfma_f32_16x16x32_bf16 v[60:63], v[144:147], v[176:179], v[60:63]
	v_mfma_f32_16x16x32_bf16 v[56:59], v[152:155], v[176:179], v[56:59]
	v_mfma_f32_16x16x32_bf16 v[52:55], v[144:147], v[184:187], v[52:55]
	v_mfma_f32_16x16x32_bf16 v[48:51], v[152:155], v[184:187], v[48:51]
	v_mfma_f32_16x16x32_bf16 v[44:47], v[144:147], v[192:195], v[44:47]
	v_mfma_f32_16x16x32_bf16 v[40:43], v[152:155], v[192:195], v[40:43]
	v_mfma_f32_16x16x32_bf16 v[36:39], v[144:147], v[200:203], v[36:39]
	v_mfma_f32_16x16x32_bf16 v[32:35], v[152:155], v[200:203], v[32:35]
	v_mfma_f32_16x16x32_bf16 v[60:63], v[148:151], v[180:183], v[60:63]
	v_mfma_f32_16x16x32_bf16 v[56:59], v[156:159], v[180:183], v[56:59]
	v_mfma_f32_16x16x32_bf16 v[52:55], v[148:151], v[188:191], v[52:55]
	v_mfma_f32_16x16x32_bf16 v[48:51], v[156:159], v[188:191], v[48:51]
	v_mfma_f32_16x16x32_bf16 v[44:47], v[148:151], v[196:199], v[44:47]
	v_mfma_f32_16x16x32_bf16 v[40:43], v[156:159], v[196:199], v[40:43]
	v_mfma_f32_16x16x32_bf16 v[36:39], v[148:151], v[204:207], v[36:39]
	v_mfma_f32_16x16x32_bf16 v[32:35], v[156:159], v[204:207], v[32:35]
	s_setprio 0
	s_setprio 1
	v_mfma_f32_16x16x32_bf16 v[28:31], v[160:163], v[176:179], v[28:31]
	v_mfma_f32_16x16x32_bf16 v[24:27], v[168:171], v[176:179], v[24:27]
	v_mfma_f32_16x16x32_bf16 v[20:23], v[160:163], v[184:187], v[20:23]
	v_mfma_f32_16x16x32_bf16 v[16:19], v[168:171], v[184:187], v[16:19]
	v_mfma_f32_16x16x32_bf16 v[12:15], v[160:163], v[192:195], v[12:15]
	v_mfma_f32_16x16x32_bf16 v[8:11], v[168:171], v[192:195], v[8:11]
	v_mfma_f32_16x16x32_bf16 v[4:7], v[160:163], v[200:203], v[4:7]
	v_mfma_f32_16x16x32_bf16 v[0:3], v[168:171], v[200:203], v[0:3]
	v_mfma_f32_16x16x32_bf16 v[28:31], v[164:167], v[180:183], v[28:31]
	v_mfma_f32_16x16x32_bf16 v[24:27], v[172:175], v[180:183], v[24:27]
	v_mfma_f32_16x16x32_bf16 v[20:23], v[164:167], v[188:191], v[20:23]
	v_mfma_f32_16x16x32_bf16 v[16:19], v[172:175], v[188:191], v[16:19]
	v_mfma_f32_16x16x32_bf16 v[12:15], v[164:167], v[196:199], v[12:15]
	v_mfma_f32_16x16x32_bf16 v[8:11], v[172:175], v[196:199], v[8:11]
	v_mfma_f32_16x16x32_bf16 v[4:7], v[164:167], v[204:207], v[4:7]
	v_mfma_f32_16x16x32_bf16 v[0:3], v[172:175], v[204:207], v[0:3]
	s_setprio 0
	s_barrier
	ds_read_b128 v[144:147], v142 offset:32768
	ds_read_b128 v[148:151], v142 offset:33792
	ds_read_b128 v[152:155], v142 offset:34816
	ds_read_b128 v[156:159], v142 offset:35840
	ds_read_b128 v[160:163], v142 offset:49152
	ds_read_b128 v[164:167], v142 offset:50176
	ds_read_b128 v[168:171], v142 offset:51200
	ds_read_b128 v[172:175], v142 offset:52224
	ds_read_b128 v[176:179], v143 offset:32768
	ds_read_b128 v[180:183], v143 offset:33792
	ds_read_b128 v[184:187], v143 offset:34816
	ds_read_b128 v[188:191], v143 offset:35840
	ds_read_b64 v[130:131], v129 offset:8
	ds_read_b128 v[192:195], v143 offset:36864
	ds_read_b128 v[196:199], v143 offset:37888
	ds_read_b128 v[200:203], v143 offset:38912
	ds_read_b128 v[204:207], v143 offset:39936
	s_mov_b32 m0, s23
	s_waitcnt lgkmcnt(4)
	buffer_load_dwordx4 v130, s[60:63], s53 offen lds
	s_mov_b32 m0, s24
	s_nop 0
	buffer_load_dwordx4 v131, s[60:63], s53 offen lds
	s_waitcnt vmcnt(8)
	s_waitcnt lgkmcnt(0)
	s_barrier
	s_setprio 1
	v_mfma_f32_16x16x32_bf16 v[124:127], v[144:147], v[176:179], v[124:127]
	v_mfma_f32_16x16x32_bf16 v[120:123], v[152:155], v[176:179], v[120:123]
	v_mfma_f32_16x16x32_bf16 v[116:119], v[144:147], v[184:187], v[116:119]
	v_mfma_f32_16x16x32_bf16 v[112:115], v[152:155], v[184:187], v[112:115]
	s_waitcnt lgkmcnt(3)
	v_mfma_f32_16x16x32_bf16 v[108:111], v[144:147], v[192:195], v[108:111]
	v_mfma_f32_16x16x32_bf16 v[104:107], v[152:155], v[192:195], v[104:107]
	s_waitcnt lgkmcnt(1)
	v_mfma_f32_16x16x32_bf16 v[100:103], v[144:147], v[200:203], v[100:103]
	v_mfma_f32_16x16x32_bf16 v[96:99], v[152:155], v[200:203], v[96:99]
	v_mfma_f32_16x16x32_bf16 v[124:127], v[148:151], v[180:183], v[124:127]
	v_mfma_f32_16x16x32_bf16 v[120:123], v[156:159], v[180:183], v[120:123]
	v_mfma_f32_16x16x32_bf16 v[116:119], v[148:151], v[188:191], v[116:119]
	v_mfma_f32_16x16x32_bf16 v[112:115], v[156:159], v[188:191], v[112:115]
	v_mfma_f32_16x16x32_bf16 v[108:111], v[148:151], v[196:199], v[108:111]
	v_mfma_f32_16x16x32_bf16 v[104:107], v[156:159], v[196:199], v[104:107]
	s_waitcnt lgkmcnt(0)
	v_mfma_f32_16x16x32_bf16 v[100:103], v[148:151], v[204:207], v[100:103]
	v_mfma_f32_16x16x32_bf16 v[96:99], v[156:159], v[204:207], v[96:99]
	s_setprio 0
	s_setprio 1
	v_mfma_f32_16x16x32_bf16 v[92:95], v[160:163], v[176:179], v[92:95]
	v_mfma_f32_16x16x32_bf16 v[88:91], v[168:171], v[176:179], v[88:91]
	v_mfma_f32_16x16x32_bf16 v[84:87], v[160:163], v[184:187], v[84:87]
	v_mfma_f32_16x16x32_bf16 v[80:83], v[168:171], v[184:187], v[80:83]
	v_mfma_f32_16x16x32_bf16 v[76:79], v[160:163], v[192:195], v[76:79]
	v_mfma_f32_16x16x32_bf16 v[72:75], v[168:171], v[192:195], v[72:75]
	v_mfma_f32_16x16x32_bf16 v[68:71], v[160:163], v[200:203], v[68:71]
	v_mfma_f32_16x16x32_bf16 v[64:67], v[168:171], v[200:203], v[64:67]
	v_mfma_f32_16x16x32_bf16 v[92:95], v[164:167], v[180:183], v[92:95]
	v_mfma_f32_16x16x32_bf16 v[88:91], v[172:175], v[180:183], v[88:91]
	v_mfma_f32_16x16x32_bf16 v[84:87], v[164:167], v[188:191], v[84:87]
	v_mfma_f32_16x16x32_bf16 v[80:83], v[172:175], v[188:191], v[80:83]
	v_mfma_f32_16x16x32_bf16 v[76:79], v[164:167], v[196:199], v[76:79]
	v_mfma_f32_16x16x32_bf16 v[72:75], v[172:175], v[196:199], v[72:75]
	v_mfma_f32_16x16x32_bf16 v[68:71], v[164:167], v[204:207], v[68:71]
	v_mfma_f32_16x16x32_bf16 v[64:67], v[172:175], v[204:207], v[64:67]
	s_setprio 0
	s_barrier
	s_mov_b32 m0, s26
	ds_read_b128 v[176:179], v143 offset:49152
	ds_read_b128 v[180:183], v143 offset:50176
	ds_read_b128 v[184:187], v143 offset:51200
	ds_read_b128 v[188:191], v143 offset:52224
	ds_read_b128 v[192:195], v143 offset:53248
	ds_read_b128 v[196:199], v143 offset:54272
	ds_read_b128 v[200:203], v143 offset:55296
	ds_read_b128 v[204:207], v143 offset:56320
	buffer_load_dwordx4 v141, s[60:63], s51 offen lds
	s_mov_b32 m0, s27
	s_nop 0
	buffer_load_dwordx4 v141, s[60:63], s52 offen lds
	s_mov_b32 m0, s30
	s_nop 0
	buffer_load_dwordx4 v141, s[60:63], s50 offen lds
	s_mov_b32 m0, s31
	s_nop 0
	buffer_load_dwordx4 v141, s[60:63], s15 offen lds
	ds_read_b64 v[130:131], v129
	s_mov_b32 m0, s28
	s_waitcnt lgkmcnt(0)
	buffer_load_dwordx4 v130, s[60:63], s14 offen lds
	s_mov_b32 m0, s29
	s_nop 0
	buffer_load_dwordx4 v131, s[60:63], s14 offen lds
	s_waitcnt vmcnt(8)
	s_waitcnt lgkmcnt(0)
	s_barrier
	s_setprio 1
	v_mfma_f32_16x16x32_bf16 v[60:63], v[144:147], v[176:179], v[60:63]
	v_mfma_f32_16x16x32_bf16 v[56:59], v[152:155], v[176:179], v[56:59]
	v_mfma_f32_16x16x32_bf16 v[52:55], v[144:147], v[184:187], v[52:55]
	v_mfma_f32_16x16x32_bf16 v[48:51], v[152:155], v[184:187], v[48:51]
	v_mfma_f32_16x16x32_bf16 v[44:47], v[144:147], v[192:195], v[44:47]
	v_mfma_f32_16x16x32_bf16 v[40:43], v[152:155], v[192:195], v[40:43]
	v_mfma_f32_16x16x32_bf16 v[36:39], v[144:147], v[200:203], v[36:39]
	v_mfma_f32_16x16x32_bf16 v[32:35], v[152:155], v[200:203], v[32:35]
	v_mfma_f32_16x16x32_bf16 v[60:63], v[148:151], v[180:183], v[60:63]
	v_mfma_f32_16x16x32_bf16 v[56:59], v[156:159], v[180:183], v[56:59]
	v_mfma_f32_16x16x32_bf16 v[52:55], v[148:151], v[188:191], v[52:55]
	v_mfma_f32_16x16x32_bf16 v[48:51], v[156:159], v[188:191], v[48:51]
	v_mfma_f32_16x16x32_bf16 v[44:47], v[148:151], v[196:199], v[44:47]
	v_mfma_f32_16x16x32_bf16 v[40:43], v[156:159], v[196:199], v[40:43]
	v_mfma_f32_16x16x32_bf16 v[36:39], v[148:151], v[204:207], v[36:39]
	v_mfma_f32_16x16x32_bf16 v[32:35], v[156:159], v[204:207], v[32:35]
	s_setprio 0
	s_setprio 1
	v_mfma_f32_16x16x32_bf16 v[28:31], v[160:163], v[176:179], v[28:31]
	v_mfma_f32_16x16x32_bf16 v[24:27], v[168:171], v[176:179], v[24:27]
	v_mfma_f32_16x16x32_bf16 v[20:23], v[160:163], v[184:187], v[20:23]
	v_mfma_f32_16x16x32_bf16 v[16:19], v[168:171], v[184:187], v[16:19]
	v_mfma_f32_16x16x32_bf16 v[12:15], v[160:163], v[192:195], v[12:15]
	v_mfma_f32_16x16x32_bf16 v[8:11], v[168:171], v[192:195], v[8:11]
	v_mfma_f32_16x16x32_bf16 v[4:7], v[160:163], v[200:203], v[4:7]
	v_mfma_f32_16x16x32_bf16 v[0:3], v[168:171], v[200:203], v[0:3]
	v_mfma_f32_16x16x32_bf16 v[28:31], v[164:167], v[180:183], v[28:31]
	v_mfma_f32_16x16x32_bf16 v[24:27], v[172:175], v[180:183], v[24:27]
	v_mfma_f32_16x16x32_bf16 v[20:23], v[164:167], v[188:191], v[20:23]
	v_mfma_f32_16x16x32_bf16 v[16:19], v[172:175], v[188:191], v[16:19]
	v_mfma_f32_16x16x32_bf16 v[12:15], v[164:167], v[196:199], v[12:15]
	v_mfma_f32_16x16x32_bf16 v[8:11], v[172:175], v[196:199], v[8:11]
	v_mfma_f32_16x16x32_bf16 v[4:7], v[164:167], v[204:207], v[4:7]
	v_mfma_f32_16x16x32_bf16 v[0:3], v[172:175], v[204:207], v[0:3]
	s_setprio 0
	s_barrier
	s_andn2_b64 vcc, exec, s[12:13]
	s_mov_b64 s[14:15], -1
	s_mov_b64 s[12:13], 0
	s_movk_i32 s50, 0x100
	s_cbranch_vccz .LBB0_696
	s_and_b64 vcc, exec, s[6:7]
	s_cbranch_vccz .LBB0_699
	s_barrier

.LBB0_949:
	s_or_b64 exec, exec, s[0:1]
	s_lshl_b32 s64, s59, 6
	s_lshl_b64 s[0:1], s[64:65], 2
	v_lshl_add_u32 v17, s14, 6, v118
	s_add_u32 s10, s72, s0
	s_mov_b32 s0, 0x2aaaaaab
	v_mul_hi_i32 v1, v17, s0
	v_lshrrev_b32_e32 v2, 31, v1
	v_ashrrev_i32_e32 v1, 1, v1
	v_add_u32_e32 v164, v1, v2
	v_mul_lo_u32 v1, v164, 12
	v_add_u32_e32 v0, 0x200, v17
	v_sub_u32_e32 v1, v17, v1
	v_lshlrev_b32_e32 v166, 3, v1
	v_mul_hi_i32 v1, v0, s0
	ds_swizzle_b32 v2, v5 offset:swizzle(SWAP,1)
	v_lshrrev_b32_e32 v3, 31, v1
	v_ashrrev_i32_e32 v1, 1, v1
	v_add_u32_e32 v168, v1, v3
	v_mul_lo_u32 v3, v168, 12
	v_sub_u32_e32 v0, v0, v3
	v_max_f32_e32 v1, v5, v5
	s_waitcnt lgkmcnt(0)
	v_max_f32_e32 v2, v2, v2
	v_lshlrev_b32_e32 v170, 3, v0
	ds_swizzle_b32 v0, v4 offset:swizzle(SWAP,1)
	v_max_f32_e32 v1, v1, v2
	ds_swizzle_b32 v2, v1 offset:swizzle(SWAP,2)
	v_max_f32_e32 v3, v4, v4
	s_addc_u32 s11, s73, s1
	s_waitcnt lgkmcnt(0)
	v_max_f32_e32 v0, v0, v0
	v_max_f32_e32 v0, v3, v0
	v_max_f32_e32 v2, v2, v2
	ds_swizzle_b32 v3, v0 offset:swizzle(SWAP,2)
	v_max_f32_e32 v1, v1, v2
	ds_swizzle_b32 v2, v1 offset:swizzle(SWAP,4)
	v_mad_i64_i32 v[174:175], s[2:3], v164, s88, 0
	s_waitcnt lgkmcnt(0)
	v_max_f32_e32 v3, v3, v3
	v_max_f32_e32 v0, v0, v3
	v_max_f32_e32 v2, v2, v2
	ds_swizzle_b32 v3, v0 offset:swizzle(SWAP,4)
	v_max_f32_e32 v1, v1, v2
	ds_swizzle_b32 v2, v1 offset:swizzle(SWAP,8)
	s_add_u32 s12, s8, 0x25c00000
	v_ashrrev_i32_e32 v16, 3, v17
	s_waitcnt lgkmcnt(0)
	v_max_f32_e32 v3, v3, v3
	v_max_f32_e32 v0, v0, v3
	v_max_f32_e32 v2, v2, v2
	ds_swizzle_b32 v3, v0 offset:swizzle(SWAP,8)
	v_max_f32_e32 v1, v1, v2
	ds_swizzle_b32 v2, v1 offset:swizzle(SWAP,16)
	v_lshlrev_b32_e32 v4, 3, v118
	s_mov_b32 s0, 0x3f828f5c
	s_waitcnt lgkmcnt(0)
	v_max_f32_e32 v3, v3, v3
	v_max_f32_e32 v0, v0, v3
	v_max_f32_e32 v2, v2, v2
	ds_swizzle_b32 v3, v0 offset:swizzle(SWAP,16)
	v_max_f32_e32 v1, v1, v2
	v_mov_b32_e32 v2, v1
	s_nop 1
	v_permlane32_swap_b32_e32 v1, v2
	v_max_f32_e32 v2, v2, v2
	v_max_f32_e32 v1, v1, v1
	v_max_f32_e32 v1, v1, v2
	s_waitcnt lgkmcnt(0)
	v_max_f32_e32 v2, v3, v3
	v_max_f32_e32 v0, v0, v2
	v_mov_b32_e32 v2, v0
	s_nop 1
	v_permlane32_swap_b32_e32 v0, v2
	v_max_f32_e32 v2, v2, v2
	v_max_f32_e32 v0, v0, v0
	v_max_f32_e32 v0, v0, v2
	v_mul_f32_e32 v1, 0x41622ae0, v1
	v_mul_f32_e32 v0, v1, v0
	s_movk_i32 s2, 0x100
	s_movk_i32 s4, 0xff
	s_addc_u32 s13, s9, 0
	v_and_b32_e32 v18, 56, v4
	v_fma_f32 v0, v0, s0, 0.5
	v_cmp_eq_u32_e64 s[0:1], 0, v17
	v_cmp_gt_i32_e64 s[2:3], s2, v17
	v_cmp_lt_i32_e64 s[4:5], s4, v17
	v_ashrrev_i32_e32 v17, 31, v16
	s_add_u32 s20, s8, 0x2ac00000
	v_lshlrev_b32_e32 v172, 1, v18
	v_and_b32_e32 v236, 0x30, v18
	v_lshlrev_b32_e32 v236, 1, v236
	v_and_b32_e32 v237, 8, v18
	v_or_b32_e32 v236, v236, v237
	v_lshlrev_b64 v[18:19], 13, v[16:17]
	v_add_u32_e32 v17, 64, v168
	s_addc_u32 s21, s9, 0
	s_lshl_b32 s22, s14, 5
	v_mad_i64_i32 v[176:177], s[14:15], v168, s88, 0
	v_mad_i64_i32 v[178:179], s[14:15], v17, s88, 0
	v_and_b32_e32 v208, 0x60, v118
	v_lshl_add_u64 v[22:23], s[8:9], 0, v[208:209]
	s_mov_b64 s[14:15], 0x200000
	v_lshl_add_u64 v[182:183], v[22:23], 0, s[14:15]
	s_mov_b64 s[14:15], 0x300000
	v_lshl_add_u64 v[184:185], v[22:23], 0, s[14:15]
	s_movk_i32 s14, 0x68
	v_mul_lo_u32 v17, v164, s14
	s_waitcnt vmcnt(0)
	v_add_lshl_u32 v161, v17, v166, 1
	v_mul_lo_u32 v17, v168, s14
	s_movk_i32 s14, 0x48
	v_mul_lo_u32 v189, v16, s14
	v_lshlrev_b32_e32 v16, 1, v189
	v_add3_u32 v220, 0, v236, v16
	v_add_u32_e32 v16, 0x80, v168
	v_lshl_add_u64 v[20:21], s[8:9], 0, v[18:19]
	v_mad_i64_i32 v[186:187], s[14:15], v16, s88, 0
	v_mov_b32_e32 v173, v209
	v_add_lshl_u32 v181, v17, v170, 1
	v_lshl_add_u64 v[16:17], v[20:21], 0, v[172:173]
	s_mov_b64 s[14:15], 0x2c400000
	v_lshl_add_u64 v[190:191], v[16:17], 0, s[14:15]
	v_and_b32_e32 v16, 7, v118
	v_lshl_or_b32 v18, v16, 4, v18
	v_ashrrev_i32_e32 v171, 31, v170
	v_lshl_add_u64 v[16:17], s[8:9], 0, v[18:19]
	s_mov_b64 s[14:15], 0x2c400180
	v_lshl_add_u64 v[192:193], v[16:17], 0, s[14:15]
	s_add_u32 s14, s8, 0x2ac09000
	v_lshlrev_b64 v[16:17], 1, v[170:171]
	v_ashrrev_i32_e32 v167, 31, v166
	s_addc_u32 s15, s9, 0
	v_mad_i64_i32 v[16:17], s[16:17], v168, s88, v[16:17]
	v_lshl_add_u64 v[194:195], s[14:15], 0, v[16:17]
	v_lshlrev_b64 v[16:17], 1, v[166:167]
	v_lshrrev_b32_e32 v24, 5, v118
	v_xor_b32_e32 v0, 0x80000000, v0
	v_mad_i64_i32 v[16:17], s[16:17], v164, s88, v[16:17]
	v_mov_b32_e32 v1, v0
	v_mov_b32_e32 v2, v0
	v_mov_b32_e32 v3, v0
	v_mov_b32_e32 v4, v0
	v_mov_b32_e32 v5, v0
	v_mov_b32_e32 v6, v0
	v_mov_b32_e32 v7, v0
	v_mov_b32_e32 v8, v0
	v_mov_b32_e32 v9, v0
	v_mov_b32_e32 v10, v0
	v_mov_b32_e32 v11, v0
	v_mov_b32_e32 v12, v0
	v_mov_b32_e32 v13, v0
	v_mov_b32_e32 v14, v0
	v_mov_b32_e32 v15, v0
	v_ashrrev_i32_e32 v165, 31, v164
	v_ashrrev_i32_e32 v169, 31, v168
	v_lshlrev_b32_e32 v180, 3, v24
	v_mov_b32_e32 v163, v209
	v_mul_u32_u24_e32 v221, 0xd0, v160
	v_mul_u32_u24_e32 v222, 0x90, v160
	v_lshlrev_b32_e32 v188, 2, v24
	v_lshl_add_u64 v[196:197], s[14:15], 0, v[16:17]
	s_branch .LBB0_952

.LBB0_961:
	s_or_b64 exec, exec, s[18:19]
	s_ashr_i32 s18, s24, 5
	s_sub_i32 s25, 15, s18
	s_and_b32 s23, s24, 7
	s_lshl_b32 s24, s25, 8
	s_add_i32 s24, s24, s22
	s_lshl_b32 s18, s26, 9
	s_and_b32 s18, s18, 0x3000
	s_ashr_i32 s19, s24, 31
	s_add_u32 s18, s24, s18
	v_or_b32_e32 v200, s18, v160
	v_mov_b64_e32 v[16:17], s[12:13]
	s_addc_u32 s26, s19, 0
	v_mad_u64_u32 v[16:17], s[18:19], v200, s54, v[16:17]
	v_mov_b32_e32 v18, 0x600
	v_mad_i32_i24 v17, s26, v18, v17
	s_mul_i32 s18, s23, 0xc0
	s_mov_b32 s19, s65
	v_lshl_add_u64 v[16:17], v[16:17], 0, s[18:19]
	v_lshlrev_b32_e32 v208, 1, v180
	v_lshl_add_u64 v[16:17], v[16:17], 0, v[208:209]
	global_load_dwordx4 v[120:123], v[16:17], off offset:128
	global_load_dwordx4 v[124:127], v[16:17], off offset:160
	global_load_dwordx4 v[130:133], v[16:17], off offset:96
	global_load_dwordx4 v[138:141], v[16:17], off offset:64
	global_load_dwordx4 v[146:149], v[16:17], off offset:32
	global_load_dwordx4 v[154:157], v[16:17], off
	s_load_dwordx2 s[18:19], s[6:7], 0x90
	v_lshlrev_b32_e32 v16, 2, v180
	v_mov_b32_e32 v17, v209
	global_load_dwordx4 v[100:103], v[198:199], off offset:128
	v_mov_b32_e32 v201, s26
	s_waitcnt lgkmcnt(0)
	v_lshl_add_u64 v[18:19], v[162:163], 2, s[18:19]
	v_lshl_add_u64 v[24:25], v[18:19], 0, v[16:17]
	global_load_dwordx4 v[76:79], v[24:25], off offset:16
	global_load_dwordx4 v[88:91], v[24:25], off
	global_load_dwordx4 v[68:71], v[24:25], off offset:80
	global_load_dwordx4 v[72:75], v[24:25], off offset:64
	global_load_dwordx4 v[60:63], v[24:25], off offset:144
	global_load_dwordx4 v[64:67], v[24:25], off offset:128
	global_load_dwordx4 v[52:55], v[24:25], off offset:208
	global_load_dwordx4 v[56:59], v[24:25], off offset:192
	global_load_dwordx4 v[16:19], v[24:25], off offset:272
	global_load_dwordx4 v[36:39], v[24:25], off offset:256
	global_load_dwordx4 v[20:23], v[24:25], off offset:336
	global_load_dwordx4 v[32:35], v[24:25], off offset:320
	v_lshlrev_b64 v[24:25], 6, v[200:201]
	v_lshl_add_u64 v[28:29], v[182:183], 0, v[24:25]
	v_lshl_add_u64 v[44:45], v[184:185], 0, v[24:25]
	global_load_dwordx4 v[24:27], v[28:29], off offset:16
	global_load_dwordx4 v[40:43], v[28:29], off
	s_nop 0
	global_load_dwordx4 v[28:31], v[44:45], off offset:16
	s_nop 0
	global_load_dwordx4 v[44:47], v[44:45], off
	s_waitcnt vmcnt(22)
	v_lshlrev_b32_e32 v108, 16, v123
	v_and_b32_e32 v109, 0xffff0000, v123
	s_waitcnt vmcnt(21)
	v_lshlrev_b32_e32 v110, 16, v127
	v_and_b32_e32 v111, 0xffff0000, v127
	v_lshlrev_b32_e32 v112, 16, v122
	s_waitcnt vmcnt(17)
	v_and_b32_e32 v153, 0xffff0000, v154
	v_lshlrev_b32_e32 v152, 16, v154
	v_mul_f32_e32 v154, v153, v153
	v_lshlrev_b32_e32 v150, 16, v155
	v_and_b32_e32 v151, 0xffff0000, v155
	v_pk_fma_f32 v[154:155], v[152:153], v[152:153], v[154:155] op_sel_hi:[1,1,0]
	v_and_b32_e32 v113, 0xffff0000, v122
	v_lshlrev_b32_e32 v114, 16, v126
	v_and_b32_e32 v115, 0xffff0000, v126
	v_lshlrev_b32_e32 v116, 16, v121
	v_and_b32_e32 v117, 0xffff0000, v121
	v_lshlrev_b32_e32 v118, 16, v125
	v_and_b32_e32 v119, 0xffff0000, v125
	v_lshlrev_b32_e32 v106, 16, v120
	v_and_b32_e32 v107, 0xffff0000, v120
	v_lshlrev_b32_e32 v120, 16, v124
	v_and_b32_e32 v121, 0xffff0000, v124
	v_lshlrev_b32_e32 v122, 16, v133
	v_and_b32_e32 v123, 0xffff0000, v133
	v_lshlrev_b32_e32 v124, 16, v132
	v_and_b32_e32 v125, 0xffff0000, v132
	v_lshlrev_b32_e32 v126, 16, v131
	v_and_b32_e32 v127, 0xffff0000, v131
	v_lshlrev_b32_e32 v128, 16, v130
	v_and_b32_e32 v129, 0xffff0000, v130
	v_lshlrev_b32_e32 v130, 16, v141
	v_and_b32_e32 v131, 0xffff0000, v141
	v_lshlrev_b32_e32 v132, 16, v140
	v_and_b32_e32 v133, 0xffff0000, v140
	v_lshlrev_b32_e32 v134, 16, v139
	v_and_b32_e32 v135, 0xffff0000, v139
	v_lshlrev_b32_e32 v136, 16, v138
	v_and_b32_e32 v137, 0xffff0000, v138
	v_lshlrev_b32_e32 v138, 16, v149
	v_and_b32_e32 v139, 0xffff0000, v149
	v_lshlrev_b32_e32 v140, 16, v148
	v_and_b32_e32 v141, 0xffff0000, v148
	v_lshlrev_b32_e32 v148, 16, v156
	v_and_b32_e32 v149, 0xffff0000, v156
	v_pk_fma_f32 v[154:155], v[150:151], v[150:151], v[154:155]
	v_mul_f32_e32 v156, v151, v151
	v_pk_add_f32 v[154:155], v[156:157], v[154:155] op_sel_hi:[0,1]
	v_pk_fma_f32 v[154:155], v[148:149], v[148:149], v[154:155]
	v_mul_f32_e32 v156, v149, v149
	v_lshlrev_b32_e32 v142, 16, v147
	v_and_b32_e32 v143, 0xffff0000, v147
	v_lshlrev_b32_e32 v144, 16, v146
	v_and_b32_e32 v145, 0xffff0000, v146
	v_lshlrev_b32_e32 v146, 16, v157
	v_and_b32_e32 v147, 0xffff0000, v157
	v_pk_add_f32 v[154:155], v[156:157], v[154:155] op_sel_hi:[0,1]
	v_pk_fma_f32 v[154:155], v[146:147], v[146:147], v[154:155]
	v_mul_f32_e32 v156, v147, v147
	v_pk_add_f32 v[154:155], v[156:157], v[154:155] op_sel_hi:[0,1]
	v_pk_fma_f32 v[154:155], v[144:145], v[144:145], v[154:155]
	v_mul_f32_e32 v156, v145, v145
	v_pk_add_f32 v[154:155], v[156:157], v[154:155] op_sel_hi:[0,1]
	v_pk_fma_f32 v[154:155], v[142:143], v[142:143], v[154:155]
	v_mul_f32_e32 v156, v143, v143
	v_pk_add_f32 v[154:155], v[156:157], v[154:155] op_sel_hi:[0,1]
	v_pk_fma_f32 v[154:155], v[140:141], v[140:141], v[154:155]
	v_mul_f32_e32 v156, v141, v141
	v_pk_add_f32 v[154:155], v[156:157], v[154:155] op_sel_hi:[0,1]
	v_pk_fma_f32 v[154:155], v[138:139], v[138:139], v[154:155]
	v_mul_f32_e32 v156, v139, v139
	v_pk_add_f32 v[154:155], v[156:157], v[154:155] op_sel_hi:[0,1]
	v_pk_fma_f32 v[154:155], v[136:137], v[136:137], v[154:155]
	v_mul_f32_e32 v156, v137, v137
	v_pk_add_f32 v[154:155], v[156:157], v[154:155] op_sel_hi:[0,1]
	v_pk_fma_f32 v[154:155], v[134:135], v[134:135], v[154:155]
	v_mul_f32_e32 v156, v135, v135
	v_pk_add_f32 v[154:155], v[156:157], v[154:155] op_sel_hi:[0,1]
	v_pk_fma_f32 v[154:155], v[132:133], v[132:133], v[154:155]
	v_mul_f32_e32 v156, v133, v133
	v_pk_add_f32 v[154:155], v[156:157], v[154:155] op_sel_hi:[0,1]
	v_pk_fma_f32 v[154:155], v[130:131], v[130:131], v[154:155]
	v_mul_f32_e32 v156, v131, v131
	v_pk_add_f32 v[154:155], v[156:157], v[154:155] op_sel_hi:[0,1]
	v_pk_fma_f32 v[154:155], v[128:129], v[128:129], v[154:155]
	v_mul_f32_e32 v156, v129, v129
	v_pk_add_f32 v[154:155], v[156:157], v[154:155] op_sel_hi:[0,1]
	v_pk_fma_f32 v[154:155], v[126:127], v[126:127], v[154:155]
	v_mul_f32_e32 v156, v127, v127
	v_pk_add_f32 v[154:155], v[156:157], v[154:155] op_sel_hi:[0,1]
	v_pk_fma_f32 v[154:155], v[124:125], v[124:125], v[154:155]
	v_mul_f32_e32 v156, v125, v125
	v_pk_add_f32 v[154:155], v[156:157], v[154:155] op_sel_hi:[0,1]
	v_pk_fma_f32 v[154:155], v[122:123], v[122:123], v[154:155]
	v_mul_f32_e32 v156, v123, v123
	v_pk_add_f32 v[154:155], v[156:157], v[154:155] op_sel_hi:[0,1]
	v_pk_fma_f32 v[154:155], v[106:107], v[106:107], v[154:155]
	v_mul_f32_e32 v156, v107, v107
	v_pk_add_f32 v[154:155], v[156:157], v[154:155] op_sel_hi:[0,1]
	v_pk_fma_f32 v[154:155], v[116:117], v[116:117], v[154:155]
	v_mul_f32_e32 v156, v117, v117
	v_pk_add_f32 v[154:155], v[156:157], v[154:155] op_sel_hi:[0,1]
	v_pk_fma_f32 v[154:155], v[112:113], v[112:113], v[154:155]
	v_mul_f32_e32 v156, v113, v113
	v_pk_add_f32 v[154:155], v[156:157], v[154:155] op_sel_hi:[0,1]
	v_pk_fma_f32 v[154:155], v[108:109], v[108:109], v[154:155]
	v_mul_f32_e32 v156, v109, v109
	v_pk_add_f32 v[154:155], v[156:157], v[154:155] op_sel_hi:[0,1]
	v_pk_fma_f32 v[154:155], v[120:121], v[120:121], v[154:155]
	v_mul_f32_e32 v156, v121, v121
	v_pk_add_f32 v[154:155], v[156:157], v[154:155] op_sel_hi:[0,1]
	v_pk_fma_f32 v[154:155], v[118:119], v[118:119], v[154:155]
	v_mul_f32_e32 v156, v119, v119
	v_pk_add_f32 v[154:155], v[156:157], v[154:155] op_sel_hi:[0,1]
	v_pk_fma_f32 v[154:155], v[114:115], v[114:115], v[154:155]
	v_mul_f32_e32 v156, v115, v115
	v_pk_add_f32 v[154:155], v[156:157], v[154:155] op_sel_hi:[0,1]
	v_pk_fma_f32 v[154:155], v[110:111], v[110:111], v[154:155]
	v_mul_f32_e32 v156, v111, v111
	v_pk_add_f32 v[154:155], v[156:157], v[154:155] op_sel_hi:[0,1]
	v_mov_b32_e32 v155, v154
	v_add_u32_e32 v156, 0, v161
	s_nop 0
	v_permlane32_swap_b32_e32 v154, v155
	ds_write_b128 v156, v[92:95]
	v_add_u32_e32 v92, 0x3400, v220
	s_and_saveexec_b64 s[18:19], s[4:5]
	s_xor_b64 s[18:19], exec, s[18:19]
	s_cbranch_execz .LBB0_963
	ds_write2_b64 v92, v[84:85], v[86:87] offset1:2
	ds_write_b128 v156, v[96:99] offset:22592
.LBB0_963:
	s_andn2_saveexec_b64 s[18:19], s[18:19]
	s_cbranch_execz .LBB0_965
	v_add_u32_e32 v93, 0, v181
	ds_write_b128 v93, v[80:83]
	ds_write2_b64 v92, v[84:85], v[86:87] offset1:2
	ds_write_b128 v156, v[96:99] offset:22592
	ds_write_b128 v93, v[48:51] offset:22592
.LBB0_965:
	s_or_b64 exec, exec, s[18:19]
	v_add_u32_e32 v80, 0x8c40, v220
	s_waitcnt vmcnt(16)
	ds_write2_b64 v80, v[100:101], v[102:103] offset1:2
	v_add_co_u32_e32 v80, vcc, 0x6000, v104
	s_nop 1
	v_addc_co_u32_e32 v81, vcc, 0, v105, vcc
	global_load_dwordx4 v[84:87], v[80:81], off
	s_and_saveexec_b64 s[18:19], s[2:3]
	s_cbranch_execz .LBB0_967
	v_lshl_add_u64 v[48:49], s[16:17], 0, v[186:187]
	v_lshl_add_u64 v[48:49], v[170:171], 1, v[48:49]
	global_load_dwordx4 v[48:51], v[48:49], off

.LBB0_968:
	s_add_i32 s29, s30, 3
	s_cmp_lt_u32 s29, s26
	s_waitcnt vmcnt(1)
	s_cselect_b64 s[14:15], -1, 0
	s_cmp_ge_u32 s29, s26
	s_cbranch_scc1 .LBB0_973
	global_load_dwordx4 v[124:127], v[218:219], off
	s_and_saveexec_b64 s[16:17], s[2:3]
	s_cbranch_execz .LBB0_971
	global_load_dwordx4 v[116:119], v[216:217], off

.LBB0_974:
	s_sub_i32 s16, s28, 64
	s_cmp_gt_i32 s16, s24
	s_cbranch_scc1 .Ltile1_diag
	s_and_b32 s16, s30, 2
	s_mulk_i32 s16, 0x5840
	v_add3_u32 v52, s16, v221, v208
	ds_read_b128 v[48:51], v52
	ds_read_b128 v[128:131], v52 offset:32
	ds_read_b128 v[140:143], v52 offset:64
	ds_read_b128 v[144:147], v52 offset:96
	ds_read_b128 v[156:159], v52 offset:128
	ds_read_b128 v[224:227], v52 offset:160
	ds_read_b128 v[132:135], v52 offset:6656
	ds_read_b128 v[136:139], v52 offset:6688
	ds_read_b128 v[148:151], v52 offset:6720
	ds_read_b128 v[152:155], v52 offset:6752
	ds_read_b128 v[228:231], v52 offset:6784
	ds_read_b128 v[232:235], v52 offset:6816
	v_add3_u32 v248, s16, v222, v208
	s_waitcnt lgkmcnt(11)
	v_mfma_f32_32x32x16_bf16 v[64:79], v[48:51], v[88:91], v[0:15]
	s_waitcnt lgkmcnt(9)
	v_mfma_f32_32x32x16_bf16 v[64:79], v[128:131], v[92:95], v[64:79]
	v_mfma_f32_32x32x16_bf16 v[64:79], v[140:143], v[96:99], v[64:79]
	s_waitcnt lgkmcnt(6)
	v_mfma_f32_32x32x16_bf16 v[64:79], v[144:147], v[100:103], v[64:79]
	v_mfma_f32_32x32x16_bf16 v[64:79], v[156:159], v[108:111], v[64:79]
	v_mfma_f32_32x32x16_bf16 v[64:79], v[224:227], v[112:115], v[64:79]
	ds_read_b128 v[156:159], v248 offset:13312
	ds_read_b128 v[144:147], v248 offset:17920
	ds_read_b128 v[140:143], v248 offset:13344
	ds_read_b128 v[128:131], v248 offset:17952
	s_waitcnt lgkmcnt(7)
	v_mfma_f32_32x32x16_bf16 v[48:63], v[132:135], v[88:91], v[0:15]
	v_mfma_f32_32x32x16_bf16 v[48:63], v[136:139], v[92:95], v[48:63]
	v_mfma_f32_32x32x16_bf16 v[48:63], v[148:151], v[96:99], v[48:63]
	s_waitcnt lgkmcnt(4)
	v_mfma_f32_32x32x16_bf16 v[48:63], v[152:155], v[100:103], v[48:63]
	s_nop 1
	v_exp_f32_e32 v64, v64
	v_exp_f32_e32 v65, v65
	v_exp_f32_e32 v66, v66
	v_exp_f32_e32 v67, v67
	v_mfma_f32_32x32x16_bf16 v[48:63], v[228:231], v[108:111], v[48:63]
	v_exp_f32_e32 v68, v68
	v_exp_f32_e32 v69, v69
	v_exp_f32_e32 v70, v70
	v_exp_f32_e32 v71, v71
	v_add_f32_e32 v212, v64, v65
	v_add_f32_e32 v213, v66, v67
	v_mfma_f32_32x32x16_bf16 v[48:63], v[232:235], v[112:115], v[48:63]
	v_exp_f32_e32 v72, v72
	v_exp_f32_e32 v73, v73
	v_exp_f32_e32 v74, v74
	v_exp_f32_e32 v75, v75
	v_add_f32_e32 v214, v68, v69
	v_add_f32_e32 v215, v70, v71
	v_exp_f32_e32 v76, v76
	v_exp_f32_e32 v77, v77
	v_exp_f32_e32 v78, v78
	v_exp_f32_e32 v79, v79
	ds_read_b128 v[132:135], v248 offset:13376
	ds_read_b128 v[136:139], v248 offset:17984
	ds_read_b128 v[148:151], v248 offset:13408
	ds_read_b128 v[152:155], v248 offset:18016
	v_cvt_pk_bf16_f32 v64, v64, v65
	v_cvt_pk_bf16_f32 v65, v66, v67
	v_cvt_pk_bf16_f32 v66, v68, v69
	v_cvt_pk_bf16_f32 v67, v70, v71
	v_add_f32_e32 v212, v212, v72
	v_add_f32_e32 v213, v213, v73
	v_add_f32_e32 v214, v214, v74
	v_add_f32_e32 v215, v215, v75
	s_waitcnt lgkmcnt(6)
	v_mfma_f32_32x32x16_bf16 v[32:47], v[156:159], v[64:67], v[32:47]
	v_add_f32_e32 v212, v212, v76
	v_add_f32_e32 v213, v213, v77
	v_add_f32_e32 v214, v214, v78
	v_add_f32_e32 v215, v215, v79
	v_mfma_f32_32x32x16_bf16 v[16:31], v[144:147], v[64:67], v[16:31]
	v_cvt_pk_bf16_f32 v68, v72, v73
	v_cvt_pk_bf16_f32 v69, v74, v75
	v_cvt_pk_bf16_f32 v70, v76, v77
	v_cvt_pk_bf16_f32 v71, v78, v79
	v_exp_f32_e32 v48, v48
	v_exp_f32_e32 v49, v49
	v_exp_f32_e32 v50, v50
	v_exp_f32_e32 v51, v51
	s_waitcnt lgkmcnt(4)
	v_mfma_f32_32x32x16_bf16 v[32:47], v[140:143], v[68:71], v[32:47]
	v_exp_f32_e32 v52, v52
	v_exp_f32_e32 v53, v53
	v_exp_f32_e32 v54, v54
	v_exp_f32_e32 v55, v55
	v_mfma_f32_32x32x16_bf16 v[16:31], v[128:131], v[68:71], v[16:31]
	v_exp_f32_e32 v56, v56
	v_exp_f32_e32 v57, v57
	v_exp_f32_e32 v58, v58
	v_exp_f32_e32 v59, v59
	v_add_f32_e32 v212, v212, v48
	v_add_f32_e32 v213, v213, v49
	v_add_f32_e32 v214, v214, v50
	v_add_f32_e32 v215, v215, v51
	v_exp_f32_e32 v60, v60
	v_exp_f32_e32 v61, v61
	v_exp_f32_e32 v62, v62
	v_exp_f32_e32 v63, v63
	v_add_f32_e32 v212, v212, v52
	v_add_f32_e32 v213, v213, v53
	v_add_f32_e32 v214, v214, v54
	v_add_f32_e32 v215, v215, v55
	v_cvt_pk_bf16_f32 v48, v48, v49
	v_cvt_pk_bf16_f32 v49, v50, v51
	v_cvt_pk_bf16_f32 v50, v52, v53
	v_cvt_pk_bf16_f32 v51, v54, v55
	v_add_f32_e32 v212, v212, v56
	v_add_f32_e32 v213, v213, v57
	v_add_f32_e32 v214, v214, v58
	v_add_f32_e32 v215, v215, v59
	s_waitcnt lgkmcnt(2)
	v_mfma_f32_32x32x16_bf16 v[32:47], v[132:135], v[48:51], v[32:47]
	v_add_f32_e32 v212, v212, v60
	v_add_f32_e32 v213, v213, v61
	v_add_f32_e32 v214, v214, v62
	v_add_f32_e32 v215, v215, v63
	v_mfma_f32_32x32x16_bf16 v[16:31], v[136:139], v[48:51], v[16:31]
	v_cvt_pk_bf16_f32 v52, v56, v57
	v_cvt_pk_bf16_f32 v53, v58, v59
	v_cvt_pk_bf16_f32 v54, v60, v61
	v_cvt_pk_bf16_f32 v55, v62, v63
	v_add_f32_e32 v212, v212, v213
	v_add_f32_e32 v214, v214, v215
	s_waitcnt lgkmcnt(0)
	v_mfma_f32_32x32x16_bf16 v[32:47], v[148:151], v[52:55], v[32:47]
	v_add_f32_e32 v212, v212, v214
	v_mfma_f32_32x32x16_bf16 v[16:31], v[152:155], v[52:55], v[16:31]
	v_add_f32_e32 v173, v173, v212
	s_branch .Ltile1_join
.Ltile1_diag:
	s_and_b32 s16, s30, 2
	s_mulk_i32 s16, 0x5840
	s_add_i32 s16, s16, 0
	v_add3_u32 v52, s16, v221, v208
	ds_read_b128 v[48:51], v52
	ds_read_b128 v[128:131], v52 offset:32
	ds_read_b128 v[132:135], v52 offset:6656
	ds_read_b128 v[136:139], v52 offset:6688
	ds_read_b128 v[140:143], v52 offset:64
	ds_read_b128 v[144:147], v52 offset:96
	ds_read_b128 v[148:151], v52 offset:6720
	ds_read_b128 v[152:155], v52 offset:6752
	ds_read_b128 v[156:159], v52 offset:128
	ds_read_b128 v[224:227], v52 offset:160
	ds_read_b128 v[228:231], v52 offset:6784
	ds_read_b128 v[232:235], v52 offset:6816
	s_waitcnt lgkmcnt(11)
	v_mfma_f32_32x32x16_bf16 v[64:79], v[48:51], v[88:91], v[0:15]
	s_waitcnt lgkmcnt(9)
	v_mfma_f32_32x32x16_bf16 v[48:63], v[132:135], v[88:91], v[0:15]
	v_mfma_f32_32x32x16_bf16 v[64:79], v[128:131], v[92:95], v[64:79]
	v_add3_u32 v128, s16, v222, v208
	s_waitcnt lgkmcnt(8)
	v_mfma_f32_32x32x16_bf16 v[48:63], v[136:139], v[92:95], v[48:63]
	s_waitcnt lgkmcnt(7)
	v_mfma_f32_32x32x16_bf16 v[64:79], v[140:143], v[96:99], v[64:79]
	s_waitcnt lgkmcnt(5)
	v_mfma_f32_32x32x16_bf16 v[48:63], v[148:151], v[96:99], v[48:63]
	v_mfma_f32_32x32x16_bf16 v[64:79], v[144:147], v[100:103], v[64:79]
	s_waitcnt lgkmcnt(4)
	v_mfma_f32_32x32x16_bf16 v[48:63], v[152:155], v[100:103], v[48:63]
	s_waitcnt lgkmcnt(3)
	v_mfma_f32_32x32x16_bf16 v[64:79], v[156:159], v[108:111], v[64:79]
	ds_read_b128 v[156:159], v128 offset:13312
	ds_read_b128 v[148:151], v128 offset:13344
	ds_read_b128 v[152:155], v128 offset:17920
	ds_read_b128 v[144:147], v128 offset:17952
	ds_read_b128 v[140:143], v128 offset:13376
	ds_read_b128 v[136:139], v128 offset:17984
	ds_read_b128 v[132:135], v128 offset:13408
	ds_read_b128 v[128:131], v128 offset:18016
	s_waitcnt lgkmcnt(9)
	v_mfma_f32_32x32x16_bf16 v[48:63], v[228:231], v[108:111], v[48:63]
	v_mfma_f32_32x32x16_bf16 v[64:79], v[224:227], v[112:115], v[64:79]
	s_waitcnt lgkmcnt(8)
	v_mfma_f32_32x32x16_bf16 v[48:63], v[232:235], v[112:115], v[48:63]
	s_sub_i32 s16, s28, 64
	s_cmp_le_i32 s16, s24
	s_cbranch_scc1 .LBB0_976
	v_add_u32_e32 v212, s28, v188
	v_add_u32_e32 v214, 0xffffffa1, v212
	v_add_u32_e32 v213, 0xffffff81, v212
	v_cmp_le_i32_e32 vcc, v214, v223
	s_nop 4
	v_cndmask_b32_e32 v48, v242, v48, vcc
	v_cmp_lt_i32_e32 vcc, v213, v223
	s_nop 1
	v_cndmask_b32_e32 v65, v242, v65, vcc
	v_cmp_le_i32_e32 vcc, v213, v223
	v_add_u32_e32 v213, 0xffffffa2, v212
	s_nop 0
	v_cndmask_b32_e32 v64, v242, v64, vcc
	v_cmp_le_i32_e32 vcc, v213, v223
	v_add_u32_e32 v213, 0xffffff83, v212
	s_nop 0
	v_cndmask_b32_e32 v49, v242, v49, vcc
	v_cmp_le_i32_e32 vcc, v213, v223
	v_add_u32_e32 v213, 0xffffffa3, v212
	s_nop 0
	v_cndmask_b32_e32 v66, v242, v66, vcc
	v_cmp_le_i32_e32 vcc, v213, v223
	v_add_u32_e32 v213, 0xffffff84, v212
	s_nop 0
	v_cndmask_b32_e32 v50, v242, v50, vcc
	v_cmp_le_i32_e32 vcc, v213, v223
	v_add_u32_e32 v213, 0xffffffa4, v212
	s_nop 0
	v_cndmask_b32_e32 v67, v242, v67, vcc
	v_cmp_le_i32_e32 vcc, v213, v223
	v_add_u32_e32 v213, 0xffffff89, v212
	s_nop 0
	v_cndmask_b32_e32 v51, v242, v51, vcc
	v_cmp_le_i32_e32 vcc, v213, v223
	v_add_u32_e32 v213, 0xffffffa9, v212
	s_nop 0
	v_cndmask_b32_e32 v68, v242, v68, vcc
	v_cmp_le_i32_e32 vcc, v213, v223
	v_add_u32_e32 v213, 0xffffff8a, v212
	s_nop 0
	v_cndmask_b32_e32 v52, v242, v52, vcc
	v_cmp_le_i32_e32 vcc, v213, v223
	v_add_u32_e32 v213, 0xffffffaa, v212
	s_nop 0
	v_cndmask_b32_e32 v69, v242, v69, vcc
	v_cmp_le_i32_e32 vcc, v213, v223
	v_add_u32_e32 v213, 0xffffff8b, v212
	s_nop 0
	v_cndmask_b32_e32 v53, v242, v53, vcc
	v_cmp_le_i32_e32 vcc, v213, v223
	v_add_u32_e32 v213, 0xffffffab, v212
	s_nop 0
	v_cndmask_b32_e32 v70, v242, v70, vcc
	v_cmp_le_i32_e32 vcc, v213, v223
	v_add_u32_e32 v213, 0xffffff8c, v212
	s_nop 0
	v_cndmask_b32_e32 v54, v242, v54, vcc
	v_cmp_le_i32_e32 vcc, v213, v223
	v_add_u32_e32 v213, 0xffffffac, v212
	s_nop 0
	v_cndmask_b32_e32 v71, v242, v71, vcc
	v_cmp_le_i32_e32 vcc, v213, v223
	v_add_u32_e32 v213, 0xffffff91, v212
	s_nop 0
	v_cndmask_b32_e32 v55, v242, v55, vcc
	v_cmp_le_i32_e32 vcc, v213, v223
	v_add_u32_e32 v213, 0xffffffb1, v212
	s_nop 0
	v_cndmask_b32_e32 v72, v242, v72, vcc
	v_cmp_le_i32_e32 vcc, v213, v223
	v_add_u32_e32 v213, 0xffffff92, v212
	s_nop 0
	v_cndmask_b32_e32 v56, v242, v56, vcc
	v_cmp_le_i32_e32 vcc, v213, v223
	v_add_u32_e32 v213, 0xffffffb2, v212
	s_nop 0
	v_cndmask_b32_e32 v73, v242, v73, vcc
	v_cmp_le_i32_e32 vcc, v213, v223
	v_add_u32_e32 v213, 0xffffff93, v212
	s_nop 0
	v_cndmask_b32_e32 v57, v242, v57, vcc
	v_cmp_le_i32_e32 vcc, v213, v223
	v_add_u32_e32 v213, 0xffffffb3, v212
	s_nop 0
	v_cndmask_b32_e32 v74, v242, v74, vcc
	v_cmp_le_i32_e32 vcc, v213, v223
	v_add_u32_e32 v213, 0xffffff94, v212
	s_nop 0
	v_cndmask_b32_e32 v58, v242, v58, vcc
	v_cmp_le_i32_e32 vcc, v213, v223
	v_add_u32_e32 v213, 0xffffffb4, v212
	s_nop 0
	v_cndmask_b32_e32 v75, v242, v75, vcc
	v_cmp_le_i32_e32 vcc, v213, v223
	v_add_u32_e32 v213, 0xffffff99, v212
	s_nop 0
	v_cndmask_b32_e32 v59, v242, v59, vcc
	v_cmp_le_i32_e32 vcc, v213, v223
	v_add_u32_e32 v213, 0xffffffb9, v212
	s_nop 0
	v_cndmask_b32_e32 v76, v242, v76, vcc
	v_cmp_le_i32_e32 vcc, v213, v223
	v_add_u32_e32 v213, 0xffffff9a, v212
	s_nop 0
	v_cndmask_b32_e32 v60, v242, v60, vcc
	v_cmp_le_i32_e32 vcc, v213, v223
	v_add_u32_e32 v213, 0xffffffba, v212
	s_nop 0
	v_cndmask_b32_e32 v77, v242, v77, vcc
	v_cmp_le_i32_e32 vcc, v213, v223
	v_add_u32_e32 v213, 0xffffff9b, v212
	s_nop 0
	v_cndmask_b32_e32 v61, v242, v61, vcc
	v_cmp_le_i32_e32 vcc, v213, v223
	v_add_u32_e32 v213, 0xffffffbb, v212
	s_nop 0
	v_cndmask_b32_e32 v78, v242, v78, vcc
	v_cmp_le_i32_e32 vcc, v213, v223
	v_add_u32_e32 v213, 0xffffff9c, v212
	v_add_u32_e32 v212, 0xffffffbc, v212
	v_cndmask_b32_e32 v62, v242, v62, vcc
	v_cmp_le_i32_e32 vcc, v213, v223
	s_nop 1
	v_cndmask_b32_e32 v79, v242, v79, vcc
	v_cmp_le_i32_e32 vcc, v212, v223
	s_nop 1
	v_cndmask_b32_e32 v63, v242, v63, vcc

.LBB0_977:
	s_and_b32 s16, s31, 2
	s_mulk_i32 s16, 0x5840
	s_add_i32 s18, s16, 0
	v_add_u32_e32 v48, s18, v161
	ds_write_b128 v48, v[84:87]
	s_and_saveexec_b64 s[16:17], s[2:3]
	v_add_u32_e32 v48, s18, v181
	ds_write_b128 v48, v[80:83]
	s_or_b64 exec, exec, s[16:17]
	v_lshl_add_u32 v48, v189, 1, s18
	v_add3_u32 v48, v48, v236, s89
	s_waitcnt vmcnt(0)
	ds_write2_b64 v48, v[104:105], v[106:107] offset1:2
.LBB0_980:
	s_waitcnt lgkmcnt(0)
	s_barrier
	s_waitcnt vmcnt(0)
	s_cmp_ge_u32 s30, s25
	s_cbranch_scc1 .LBB0_985
	s_add_i32 s64, s30, 4
	s_lshl_b64 s[16:17], s[64:65], 6
	v_lshl_add_u64 v[48:49], s[16:17], 0, v[164:165]
	v_mad_u64_u32 v[50:51], s[18:19], v48, s88, v[202:203]
	v_mad_i32_i24 v51, v49, s88, v51
	global_load_dwordx4 v[84:87], v[50:51], off
	s_and_saveexec_b64 s[18:19], s[2:3]
	s_cbranch_execz .LBB0_983
	v_lshl_add_u64 v[48:49], s[16:17], 0, v[168:169]
	v_mad_u64_u32 v[50:51], s[34:35], v48, s88, v[204:205]
	v_mad_i32_i24 v51, v49, s88, v51
	global_load_dwordx4 v[80:83], v[50:51], off

.LBB0_986:
	s_cmp_gt_i32 s28, s24
	s_cbranch_scc1 .Ltile2_diag
	s_add_i32 s16, s30, 1
	s_and_b32 s16, s16, 3
	s_mulk_i32 s16, 0x5840
	v_add3_u32 v52, s16, v221, v208
	ds_read_b128 v[48:51], v52
	ds_read_b128 v[128:131], v52 offset:32
	ds_read_b128 v[140:143], v52 offset:64
	ds_read_b128 v[144:147], v52 offset:96
	ds_read_b128 v[156:159], v52 offset:128
	ds_read_b128 v[224:227], v52 offset:160
	ds_read_b128 v[132:135], v52 offset:6656
	ds_read_b128 v[136:139], v52 offset:6688
	ds_read_b128 v[148:151], v52 offset:6720
	ds_read_b128 v[152:155], v52 offset:6752
	ds_read_b128 v[228:231], v52 offset:6784
	ds_read_b128 v[232:235], v52 offset:6816
	v_add3_u32 v248, s16, v222, v208
	s_waitcnt lgkmcnt(11)
	v_mfma_f32_32x32x16_bf16 v[64:79], v[48:51], v[88:91], v[0:15]
	s_waitcnt lgkmcnt(9)
	v_mfma_f32_32x32x16_bf16 v[64:79], v[128:131], v[92:95], v[64:79]
	v_mfma_f32_32x32x16_bf16 v[64:79], v[140:143], v[96:99], v[64:79]
	s_waitcnt lgkmcnt(6)
	v_mfma_f32_32x32x16_bf16 v[64:79], v[144:147], v[100:103], v[64:79]
	v_mfma_f32_32x32x16_bf16 v[64:79], v[156:159], v[108:111], v[64:79]
	v_mfma_f32_32x32x16_bf16 v[64:79], v[224:227], v[112:115], v[64:79]
	ds_read_b128 v[156:159], v248 offset:13312
	ds_read_b128 v[144:147], v248 offset:17920
	ds_read_b128 v[140:143], v248 offset:13344
	ds_read_b128 v[128:131], v248 offset:17952
	s_waitcnt lgkmcnt(7)
	v_mfma_f32_32x32x16_bf16 v[48:63], v[132:135], v[88:91], v[0:15]
	v_mfma_f32_32x32x16_bf16 v[48:63], v[136:139], v[92:95], v[48:63]
	v_mfma_f32_32x32x16_bf16 v[48:63], v[148:151], v[96:99], v[48:63]
	s_waitcnt lgkmcnt(4)
	v_mfma_f32_32x32x16_bf16 v[48:63], v[152:155], v[100:103], v[48:63]
	s_nop 1
	v_exp_f32_e32 v64, v64
	v_exp_f32_e32 v65, v65
	v_exp_f32_e32 v66, v66
	v_exp_f32_e32 v67, v67
	v_mfma_f32_32x32x16_bf16 v[48:63], v[228:231], v[108:111], v[48:63]
	v_exp_f32_e32 v68, v68
	v_exp_f32_e32 v69, v69
	v_exp_f32_e32 v70, v70
	v_exp_f32_e32 v71, v71
	v_add_f32_e32 v212, v64, v65
	v_add_f32_e32 v213, v66, v67
	v_mfma_f32_32x32x16_bf16 v[48:63], v[232:235], v[112:115], v[48:63]
	v_exp_f32_e32 v72, v72
	v_exp_f32_e32 v73, v73
	v_exp_f32_e32 v74, v74
	v_exp_f32_e32 v75, v75
	v_add_f32_e32 v214, v68, v69
	v_add_f32_e32 v215, v70, v71
	v_exp_f32_e32 v76, v76
	v_exp_f32_e32 v77, v77
	v_exp_f32_e32 v78, v78
	v_exp_f32_e32 v79, v79
	ds_read_b128 v[132:135], v248 offset:13376
	ds_read_b128 v[136:139], v248 offset:17984
	ds_read_b128 v[148:151], v248 offset:13408
	ds_read_b128 v[152:155], v248 offset:18016
	v_cvt_pk_bf16_f32 v64, v64, v65
	v_cvt_pk_bf16_f32 v65, v66, v67
	v_cvt_pk_bf16_f32 v66, v68, v69
	v_cvt_pk_bf16_f32 v67, v70, v71
	v_add_f32_e32 v212, v212, v72
	v_add_f32_e32 v213, v213, v73
	v_add_f32_e32 v214, v214, v74
	v_add_f32_e32 v215, v215, v75
	s_waitcnt lgkmcnt(6)
	v_mfma_f32_32x32x16_bf16 v[32:47], v[156:159], v[64:67], v[32:47]
	v_add_f32_e32 v212, v212, v76
	v_add_f32_e32 v213, v213, v77
	v_add_f32_e32 v214, v214, v78
	v_add_f32_e32 v215, v215, v79
	v_mfma_f32_32x32x16_bf16 v[16:31], v[144:147], v[64:67], v[16:31]
	v_cvt_pk_bf16_f32 v68, v72, v73
	v_cvt_pk_bf16_f32 v69, v74, v75
	v_cvt_pk_bf16_f32 v70, v76, v77
	v_cvt_pk_bf16_f32 v71, v78, v79
	v_exp_f32_e32 v48, v48
	v_exp_f32_e32 v49, v49
	v_exp_f32_e32 v50, v50
	v_exp_f32_e32 v51, v51
	s_waitcnt lgkmcnt(4)
	v_mfma_f32_32x32x16_bf16 v[32:47], v[140:143], v[68:71], v[32:47]
	v_exp_f32_e32 v52, v52
	v_exp_f32_e32 v53, v53
	v_exp_f32_e32 v54, v54
	v_exp_f32_e32 v55, v55
	v_mfma_f32_32x32x16_bf16 v[16:31], v[128:131], v[68:71], v[16:31]
	v_exp_f32_e32 v56, v56
	v_exp_f32_e32 v57, v57
	v_exp_f32_e32 v58, v58
	v_exp_f32_e32 v59, v59
	v_add_f32_e32 v212, v212, v48
	v_add_f32_e32 v213, v213, v49
	v_add_f32_e32 v214, v214, v50
	v_add_f32_e32 v215, v215, v51
	v_exp_f32_e32 v60, v60
	v_exp_f32_e32 v61, v61
	v_exp_f32_e32 v62, v62
	v_exp_f32_e32 v63, v63
	v_add_f32_e32 v212, v212, v52
	v_add_f32_e32 v213, v213, v53
	v_add_f32_e32 v214, v214, v54
	v_add_f32_e32 v215, v215, v55
	v_cvt_pk_bf16_f32 v48, v48, v49
	v_cvt_pk_bf16_f32 v49, v50, v51
	v_cvt_pk_bf16_f32 v50, v52, v53
	v_cvt_pk_bf16_f32 v51, v54, v55
	v_add_f32_e32 v212, v212, v56
	v_add_f32_e32 v213, v213, v57
	v_add_f32_e32 v214, v214, v58
	v_add_f32_e32 v215, v215, v59
	s_waitcnt lgkmcnt(2)
	v_mfma_f32_32x32x16_bf16 v[32:47], v[132:135], v[48:51], v[32:47]
	v_add_f32_e32 v212, v212, v60
	v_add_f32_e32 v213, v213, v61
	v_add_f32_e32 v214, v214, v62
	v_add_f32_e32 v215, v215, v63
	v_mfma_f32_32x32x16_bf16 v[16:31], v[136:139], v[48:51], v[16:31]
	v_cvt_pk_bf16_f32 v52, v56, v57
	v_cvt_pk_bf16_f32 v53, v58, v59
	v_cvt_pk_bf16_f32 v54, v60, v61
	v_cvt_pk_bf16_f32 v55, v62, v63
	v_add_f32_e32 v212, v212, v213
	v_add_f32_e32 v214, v214, v215
	s_waitcnt lgkmcnt(0)
	v_mfma_f32_32x32x16_bf16 v[32:47], v[148:151], v[52:55], v[32:47]
	v_add_f32_e32 v212, v212, v214
	v_mfma_f32_32x32x16_bf16 v[16:31], v[152:155], v[52:55], v[16:31]
	v_add_f32_e32 v173, v173, v212
	s_branch .Ltile2_join
.Ltile2_diag:
	s_add_i32 s16, s30, 1
	s_and_b32 s16, s16, 3
	s_mulk_i32 s16, 0x5840
	s_add_i32 s16, s16, 0
	v_add3_u32 v52, s16, v221, v208
	ds_read_b128 v[48:51], v52
	ds_read_b128 v[128:131], v52 offset:32
	ds_read_b128 v[132:135], v52 offset:6656
	ds_read_b128 v[136:139], v52 offset:6688
	ds_read_b128 v[140:143], v52 offset:64
	ds_read_b128 v[144:147], v52 offset:96
	ds_read_b128 v[148:151], v52 offset:6720
	ds_read_b128 v[152:155], v52 offset:6752
	ds_read_b128 v[156:159], v52 offset:128
	ds_read_b128 v[224:227], v52 offset:160
	ds_read_b128 v[228:231], v52 offset:6784
	ds_read_b128 v[232:235], v52 offset:6816
	s_waitcnt lgkmcnt(11)
	v_mfma_f32_32x32x16_bf16 v[64:79], v[48:51], v[88:91], v[0:15]
	s_waitcnt lgkmcnt(9)
	v_mfma_f32_32x32x16_bf16 v[48:63], v[132:135], v[88:91], v[0:15]
	v_mfma_f32_32x32x16_bf16 v[64:79], v[128:131], v[92:95], v[64:79]
	v_add3_u32 v128, s16, v222, v208
	s_waitcnt lgkmcnt(8)
	v_mfma_f32_32x32x16_bf16 v[48:63], v[136:139], v[92:95], v[48:63]
	s_waitcnt lgkmcnt(7)
	v_mfma_f32_32x32x16_bf16 v[64:79], v[140:143], v[96:99], v[64:79]
	s_waitcnt lgkmcnt(5)
	v_mfma_f32_32x32x16_bf16 v[48:63], v[148:151], v[96:99], v[48:63]
	v_mfma_f32_32x32x16_bf16 v[64:79], v[144:147], v[100:103], v[64:79]
	s_waitcnt lgkmcnt(4)
	v_mfma_f32_32x32x16_bf16 v[48:63], v[152:155], v[100:103], v[48:63]
	s_waitcnt lgkmcnt(3)
	v_mfma_f32_32x32x16_bf16 v[64:79], v[156:159], v[108:111], v[64:79]
	ds_read_b128 v[156:159], v128 offset:13312
	ds_read_b128 v[148:151], v128 offset:13344
	ds_read_b128 v[152:155], v128 offset:17920
	ds_read_b128 v[144:147], v128 offset:17952
	ds_read_b128 v[140:143], v128 offset:13376
	ds_read_b128 v[136:139], v128 offset:17984
	ds_read_b128 v[132:135], v128 offset:13408
	ds_read_b128 v[128:131], v128 offset:18016
	s_waitcnt lgkmcnt(9)
	v_mfma_f32_32x32x16_bf16 v[48:63], v[228:231], v[108:111], v[48:63]
	v_mfma_f32_32x32x16_bf16 v[64:79], v[224:227], v[112:115], v[64:79]
	s_waitcnt lgkmcnt(8)
	v_mfma_f32_32x32x16_bf16 v[48:63], v[232:235], v[112:115], v[48:63]
	s_cmp_le_i32 s28, s24
	s_cbranch_scc1 .LBB0_988
	v_add_u32_e32 v212, s28, v188
	v_subrev_u32_e32 v214, 31, v212
	v_subrev_u32_e32 v213, 63, v212
	v_cmp_le_i32_e32 vcc, v214, v223
	s_nop 5
	v_cndmask_b32_e32 v48, v242, v48, vcc
	v_cmp_lt_i32_e32 vcc, v213, v223
	s_nop 1
	v_cndmask_b32_e32 v65, v242, v65, vcc
	v_cmp_le_i32_e32 vcc, v213, v223
	v_subrev_u32_e32 v213, 30, v212
	s_nop 0
	v_cndmask_b32_e32 v64, v242, v64, vcc
	v_cmp_le_i32_e32 vcc, v213, v223
	v_subrev_u32_e32 v213, 61, v212
	s_nop 0
	v_cndmask_b32_e32 v49, v242, v49, vcc
	v_cmp_le_i32_e32 vcc, v213, v223
	v_subrev_u32_e32 v213, 29, v212
	s_nop 0
	v_cndmask_b32_e32 v66, v242, v66, vcc
	v_cmp_le_i32_e32 vcc, v213, v223
	v_subrev_u32_e32 v213, 60, v212
	s_nop 0
	v_cndmask_b32_e32 v50, v242, v50, vcc
	v_cmp_le_i32_e32 vcc, v213, v223
	v_subrev_u32_e32 v213, 28, v212
	s_nop 0
	v_cndmask_b32_e32 v67, v242, v67, vcc
	v_cmp_le_i32_e32 vcc, v213, v223
	v_subrev_u32_e32 v213, 55, v212
	s_nop 0
	v_cndmask_b32_e32 v51, v242, v51, vcc
	v_cmp_le_i32_e32 vcc, v213, v223
	v_subrev_u32_e32 v213, 23, v212
	s_nop 0
	v_cndmask_b32_e32 v68, v242, v68, vcc
	v_cmp_le_i32_e32 vcc, v213, v223
	v_subrev_u32_e32 v213, 54, v212
	s_nop 0
	v_cndmask_b32_e32 v52, v242, v52, vcc
	v_cmp_le_i32_e32 vcc, v213, v223
	v_subrev_u32_e32 v213, 22, v212
	s_nop 0
	v_cndmask_b32_e32 v69, v242, v69, vcc
	v_cmp_le_i32_e32 vcc, v213, v223
	v_subrev_u32_e32 v213, 53, v212
	s_nop 0
	v_cndmask_b32_e32 v53, v242, v53, vcc
	v_cmp_le_i32_e32 vcc, v213, v223
	v_subrev_u32_e32 v213, 21, v212
	s_nop 0
	v_cndmask_b32_e32 v70, v242, v70, vcc
	v_cmp_le_i32_e32 vcc, v213, v223
	v_subrev_u32_e32 v213, 52, v212
	s_nop 0
	v_cndmask_b32_e32 v54, v242, v54, vcc
	v_cmp_le_i32_e32 vcc, v213, v223
	v_subrev_u32_e32 v213, 20, v212
	s_nop 0
	v_cndmask_b32_e32 v71, v242, v71, vcc
	v_cmp_le_i32_e32 vcc, v213, v223
	v_subrev_u32_e32 v213, 47, v212
	s_nop 0
	v_cndmask_b32_e32 v55, v242, v55, vcc
	v_cmp_le_i32_e32 vcc, v213, v223
	v_add_u32_e32 v213, -15, v212
	s_nop 0
	v_cndmask_b32_e32 v72, v242, v72, vcc
	v_cmp_le_i32_e32 vcc, v213, v223
	v_subrev_u32_e32 v213, 46, v212
	s_nop 0
	v_cndmask_b32_e32 v56, v242, v56, vcc
	v_cmp_le_i32_e32 vcc, v213, v223
	v_add_u32_e32 v213, -14, v212
	s_nop 0
	v_cndmask_b32_e32 v73, v242, v73, vcc
	v_cmp_le_i32_e32 vcc, v213, v223
	v_subrev_u32_e32 v213, 45, v212
	s_nop 0
	v_cndmask_b32_e32 v57, v242, v57, vcc
	v_cmp_le_i32_e32 vcc, v213, v223
	v_add_u32_e32 v213, -13, v212
	s_nop 0
	v_cndmask_b32_e32 v74, v242, v74, vcc
	v_cmp_le_i32_e32 vcc, v213, v223
	v_subrev_u32_e32 v213, 44, v212
	s_nop 0
	v_cndmask_b32_e32 v58, v242, v58, vcc
	v_cmp_le_i32_e32 vcc, v213, v223
	v_add_u32_e32 v213, -12, v212
	s_nop 0
	v_cndmask_b32_e32 v75, v242, v75, vcc
	v_cmp_le_i32_e32 vcc, v213, v223
	v_subrev_u32_e32 v213, 39, v212
	s_nop 0
	v_cndmask_b32_e32 v59, v242, v59, vcc
	v_cmp_le_i32_e32 vcc, v213, v223
	v_add_u32_e32 v213, -7, v212
	s_nop 0
	v_cndmask_b32_e32 v76, v242, v76, vcc
	v_cmp_le_i32_e32 vcc, v213, v223
	v_subrev_u32_e32 v213, 38, v212
	s_nop 0
	v_cndmask_b32_e32 v60, v242, v60, vcc
	v_cmp_le_i32_e32 vcc, v213, v223
	v_add_u32_e32 v213, -6, v212
	s_nop 0
	v_cndmask_b32_e32 v77, v242, v77, vcc
	v_cmp_le_i32_e32 vcc, v213, v223
	v_subrev_u32_e32 v213, 37, v212
	s_nop 0
	v_cndmask_b32_e32 v61, v242, v61, vcc
	v_cmp_le_i32_e32 vcc, v213, v223
	v_add_u32_e32 v213, -5, v212
	s_nop 0
	v_cndmask_b32_e32 v78, v242, v78, vcc
	v_cmp_le_i32_e32 vcc, v213, v223
	v_subrev_u32_e32 v213, 36, v212
	v_add_u32_e32 v212, -4, v212
	v_cndmask_b32_e32 v62, v242, v62, vcc
	v_cmp_le_i32_e32 vcc, v213, v223
	s_nop 1
	v_cndmask_b32_e32 v79, v242, v79, vcc
	v_cmp_le_i32_e32 vcc, v212, v223
	s_nop 1
	v_cndmask_b32_e32 v63, v242, v63, vcc

.LBB0_989:
	s_and_b32 s14, s29, 3
	s_mulk_i32 s14, 0x5840
	s_add_i32 s16, s14, 0
	v_add_u32_e32 v48, s16, v161
	ds_write_b128 v48, v[124:127]
	s_and_saveexec_b64 s[14:15], s[2:3]
	v_add_u32_e32 v48, s16, v181
	ds_write_b128 v48, v[116:119]
	s_or_b64 exec, exec, s[14:15]
	v_lshl_add_u32 v48, v189, 1, s16
	v_add3_u32 v48, v48, v236, s89
	ds_write2_b64 v48, v[120:121], v[122:123] offset1:2
